# leader path: no final wait for the fire-and-forget release atomics before leaving the barrier
# speedup vs baseline: 1.0047x; 1.0047x over previous
.LBB0_119:
	s_or_b64 exec, exec, s[6:7]
	s_mov_b64 s[6:7], exec
	v_mbcnt_lo_u32_b32 v0, s6, 0
	v_mbcnt_hi_u32_b32 v0, s7, v0
	s_mov_b32 s11, 0
	v_cmp_eq_u32_e32 vcc, 0, v0
	s_and_saveexec_b64 s[8:9], vcc
	s_cbranch_execz .LBB0_121
.LBB0_121:
	s_or_b64 exec, exec, s[8:9]
.LBB0_122:
	s_or_b64 exec, exec, s[0:1]
	s_mov_b64 s[0:1], 0x5a00100
	v_writelane_b32 v255, s0, 10
	s_mov_b32 s25, 0
	s_movk_i32 s70, 0x2000
	v_writelane_b32 v255, s1, 11
	s_add_i32 s0, 0, 0xffffd800
	s_mov_b32 s31, 0x8800
	s_waitcnt lgkmcnt(0)
	v_mov_b32_e32 v0, 0
	s_movk_i32 s71, 0x100
	s_movk_i32 s72, 0x6000
	s_mov_b64 s[28:29], 0x1000
	s_movk_i32 s78, 0x1000
	s_mov_b32 s30, 0x3d800000
	s_mov_b32 s79, 0x18200000
	v_mov_b32_e32 v210, 0x358637bd
	s_mov_b64 s[34:35], 0x800
	s_mov_b32 s67, 0x10000
	s_mov_b64 s[36:37], 0x20000
	s_mov_b64 s[38:39], 0x80
	s_mov_b64 s[40:41], 0x20080
	s_movk_i32 s57, 0x300
	s_movk_i32 s60, 0x1600
	s_mov_b32 s44, 0x22000
	s_mov_b32 s53, 0x3af80000
	s_mov_b32 s55, 0x6040200
	v_writelane_b32 v255, s0, 12
	v_mov_b32_e32 v213, 0x44800000
	v_mov_b32_e32 v211, 0x7f800000
	s_mov_b64 s[42:43], 0x100
	s_mov_b32 s46, 0x3b000000
	s_mov_b64 s[74:75], 0x18000
	s_mov_b64 s[76:77], 0x18080
	s_mov_b32 s4, s25
	s_barrier
	s_branch .LBB0_125
.LBB0_123:
	s_or_b64 exec, exec, s[8:9]
.LBB0_124:
	s_or_b64 exec, exec, s[0:1]
	v_readlane_b32 s4, v255, 13
	s_add_i32 s4, s4, 1
	v_readlane_b32 s0, v255, 10
	v_readlane_b32 s1, v255, 11
	s_add_u32 s0, s0, 0x100000
	s_addc_u32 s1, s1, 0
	v_readlane_b32 s5, v255, 14
	v_writelane_b32 v255, s0, 10
	s_cmp_eq_u32 s4, 4
	s_waitcnt lgkmcnt(0)
	v_writelane_b32 v255, s1, 11
	s_barrier
	s_cbranch_scc0 .LBB0_125
	s_getpc_b64 s[98:99]

.LBB0_223:
	s_or_b64 exec, exec, s[6:7]
	s_mov_b64 s[6:7], exec
	v_mbcnt_lo_u32_b32 v1, s6, 0
	v_mbcnt_hi_u32_b32 v1, s7, v1
	v_cmp_eq_u32_e32 vcc, 0, v1
	s_and_saveexec_b64 s[8:9], vcc
	s_cbranch_execz .LBB0_225
.LBB0_225:
	s_or_b64 exec, exec, s[8:9]
.LBB0_226:
	s_or_b64 exec, exec, s[0:1]
	s_mov_b32 s10, 1
	s_waitcnt lgkmcnt(0)
	s_barrier
	s_cmp_lt_i32 s10, 1
	s_cbranch_scc1 .LBB0_269
	s_mov_b32 s11, 0
	v_writelane_b32 v255, s10, 17
	s_branch .LBB0_230

.LBB0_320:
	s_or_b64 exec, exec, s[8:9]
.LBB0_321:
	s_or_b64 exec, exec, s[0:1]
	s_mov_b32 s2, 1
	s_waitcnt lgkmcnt(0)
	s_barrier
	s_cmp_lt_i32 s2, 1
	s_cbranch_scc1 .LBB0_340
	v_readlane_b32 s0, v255, 13
	v_readlane_b32 s1, v255, 14
	s_lshl_b32 s24, s0, 2
	s_mov_b32 s3, 0
	s_lshl_b64 s[0:1], s[24:25], 2
	s_branch .LBB0_324

.LBB0_391:
	s_or_b64 exec, exec, s[8:9]
.LBB0_392:
	s_or_b64 exec, exec, s[0:1]
	v_readlane_b32 s0, v255, 13
	s_cmp_eq_u32 s0, 3
	s_cselect_b64 s[2:3], -1, 0
	v_readlane_b32 s1, v255, 14
	v_writelane_b32 v255, s2, 19
	s_cmp_lg_u32 s0, 3
	s_cselect_b64 s[0:1], -1, 0
	v_writelane_b32 v255, s3, 20
	v_writelane_b32 v255, s0, 17
	s_mov_b32 s18, 1
	s_waitcnt lgkmcnt(0)
	v_writelane_b32 v255, s1, 18
	s_barrier
	s_cmp_lt_i32 s18, 1
	s_cbranch_scc1 .LBB0_486
	v_readlane_b32 s0, v255, 13
	s_mov_b32 s2, s0
	v_cvt_f32_u32_e32 v1, s2
	s_mov_b32 s0, 0x3fb8aa3b
	s_lshl_b32 s19, s2, 2
	s_lshl_b32 s24, s2, 8
	v_mul_f32_e32 v1, 0xbe99999a, v1
	v_mul_f32_e32 v2, 0x3fb8aa3b, v1
	v_fma_f32 v3, v1, s0, -v2
	v_rndne_f32_e32 v4, v2
	v_fmac_f32_e32 v3, 0x32a5705f, v1
	v_sub_f32_e32 v2, v2, v4
	v_add_f32_e32 v2, v2, v3
	v_cvt_i32_f32_e32 v4, v4
	v_exp_f32_e32 v2, v2
	s_mov_b32 s0, 0xc2ce8ed0
	v_cmp_ngt_f32_e32 vcc, s0, v1
	s_mov_b32 s0, 0x42b17218
	v_ldexp_f32 v2, v2, v4
	v_cndmask_b32_e32 v2, 0, v2, vcc
	v_cmp_nlt_f32_e32 vcc, s0, v1
	s_lshl_b32 s0, s2, 7
	v_readlane_b32 s2, v255, 19
	v_readlane_b32 s3, v255, 20
	v_readlane_b32 s1, v255, 14
	s_and_b64 s[2:3], s[2:3], exec
	s_mov_b32 s1, s25
	s_movk_i32 s2, 0x440
	v_cndmask_b32_e32 v1, v211, v2, vcc
	v_mov_b32_e32 v2, 0x3f4ccccd
	s_cselect_b32 s86, 0x400, s2
	s_lshl_b64 s[0:1], s[0:1], 2
	v_fmamk_f32 v204, v1, 0xbf19999a, v2
	v_writelane_b32 v255, s0, 21
	v_sub_f32_e32 v205, 1.0, v204
	s_mov_b32 s87, 0
	s_lshl_b64 s[12:13], s[24:25], 2
	v_writelane_b32 v255, s1, 22
	s_branch .LBB0_395

.LBB0_535:
	s_or_b64 exec, exec, s[6:7]
	s_mov_b64 s[6:7], exec
	v_mbcnt_lo_u32_b32 v1, s6, 0
	v_mbcnt_hi_u32_b32 v1, s7, v1
	v_cmp_eq_u32_e32 vcc, 0, v1
	s_and_saveexec_b64 s[12:13], vcc
	s_cbranch_execz .LBB0_537
.LBB0_537:
	s_or_b64 exec, exec, s[12:13]
.LBB0_538:
	s_or_b64 exec, exec, s[0:1]
	v_readlane_b32 s0, v255, 13
	v_readlane_b32 s1, v255, 14
	s_mul_hi_u32 s1, s0, 0x36000
	s_mov_b32 s61, 1
	v_writelane_b32 v255, s1, 21
	s_mul_i32 s0, s0, 0x36000
	s_waitcnt lgkmcnt(0)
	s_barrier
	s_cmp_lt_i32 s61, 1
	v_writelane_b32 v255, s0, 23
	s_cbranch_scc1 .LBB0_626
	v_readlane_b32 s2, v255, 19
	v_readlane_b32 s3, v255, 20
	v_readlane_b32 s4, v255, 13
	s_xor_b64 s[50:51], s[2:3], -1
	v_readlane_b32 s5, v255, 14
	s_and_b64 s[0:1], s[2:3], exec
	s_mov_b32 s5, s25
	s_cselect_b32 s12, 0, 32
	s_lshl_b64 s[6:7], s[4:5], 20
	v_writelane_b32 v255, s6, 24
	s_lshl_b32 s0, s4, 6
	v_cndmask_b32_e64 v1, 0, 1, s[2:3]
	s_lshl_b32 s54, s4, 2
	s_lshl_b32 s24, s4, 8
	s_lshl_b32 s2, s4, 14
	v_writelane_b32 v255, s7, 25
	s_mov_b32 s6, s4
	v_writelane_b32 v255, s6, 13
	s_cmp_lg_u32 s4, 0
	s_cselect_b64 s[4:5], -1, 0
	v_writelane_b32 v255, s7, 14
	s_mov_b32 s1, s25
	v_writelane_b32 v255, s4, 26
	s_mov_b32 s17, 0
	v_readfirstlane_b32 s52, v1
	v_writelane_b32 v255, s5, 27
	s_lshl_b64 s[62:63], s[0:1], 2
	s_lshl_b32 s56, s2, 1
	s_branch .LBB0_542

.LBB0_677:
	s_or_b64 exec, exec, s[12:13]
.LBB0_678:
	s_or_b64 exec, exec, s[0:1]
	s_mov_b32 s10, 1
	s_waitcnt lgkmcnt(0)
	s_barrier
	s_cmp_lt_i32 s10, 1
	s_cbranch_scc1 .LBB0_710
	s_mov_b32 s49, s25
	s_lshl_b64 s[0:1], s[48:49], 20
	v_writelane_b32 v255, s0, 26
	s_cmp_lg_u32 s48, 0
	s_mov_b32 s3, 0
	v_writelane_b32 v255, s1, 27
	v_writelane_b32 v255, s48, 13
	s_cselect_b64 s[16:17], -1, 0
	s_nop 0
	v_writelane_b32 v255, s49, 14
	v_writelane_b32 v255, s10, 24
	s_branch .LBB0_682

.LBB0_761:
	s_or_b64 exec, exec, s[8:9]
.LBB0_762:
	v_writelane_b32 v255, s48, 13
	s_nop 1
	v_writelane_b32 v255, s49, 14
	s_or_b64 exec, exec, s[0:1]
	s_mov_b32 s62, 1
	s_waitcnt lgkmcnt(0)
	s_barrier
	s_cmp_lt_i32 s62, 1
	s_cbranch_scc1 .LBB0_976
	v_readlane_b32 s2, v255, 15
	v_readlane_b32 s3, v255, 16
	v_readlane_b32 s0, v255, 13
	s_mov_b32 s3, s25
	v_readlane_b32 s1, v255, 14
	s_lshl_b32 s24, s0, 10
	s_lshl_b64 s[0:1], s[2:3], 2
	v_writelane_b32 v255, s0, 19
	s_mov_b32 s19, 0
	s_nop 0
	v_writelane_b32 v255, s1, 20
	s_branch .LBB0_765

.LBB0_1027:
	s_or_b64 exec, exec, s[8:9]
.LBB0_1028:
	s_or_b64 exec, exec, s[0:1]
	s_mov_b32 s0, 1
	s_waitcnt lgkmcnt(0)
	s_barrier
	s_cmp_lt_i32 s0, 1
	v_writelane_b32 v255, s0, 17
	s_cbranch_scc1 .LBB0_1144
	v_readlane_b32 s0, v255, 13
	s_mov_b32 s2, s0
	s_lshl_b32 s0, s0, 10
	v_readlane_b32 s1, v255, 14
	v_writelane_b32 v255, s0, 19
	s_lshl_b32 s0, s2, 4
	s_mul_hi_u32 s1, s0, 0x180000
	v_writelane_b32 v255, s1, 21
	s_lshl_b32 s24, s2, 13
	s_mul_hi_u32 s0, s0, 0xc0000
	v_writelane_b32 v255, s0, 23
	s_mov_b32 s58, 0
	s_lshl_b64 s[80:81], s[24:25], 2
	s_branch .LBB0_1032

.LBB0_1193:
	s_or_b64 exec, exec, s[6:7]
	s_mov_b64 s[6:7], exec
	v_mbcnt_lo_u32_b32 v1, s6, 0
	v_mbcnt_hi_u32_b32 v1, s7, v1
	v_cmp_eq_u32_e32 vcc, 0, v1
	s_and_saveexec_b64 s[8:9], vcc
	s_cbranch_execnz .LBB0_1194
	s_getpc_b64 s[98:99]
